# NA phase layers 0-2: bias-table dword load issued ahead of the V staging loads (same batch), generic copy loop removed
# baseline (speedup 1.0000x reference)
.LBB0_395:
	v_med3_u32 v2, s68, 4, 28
	s_and_b32 s71, s50, 3
	v_readfirstlane_b32 s72, v2
	s_add_i32 s72, s72, -4
	v_cmp_gt_i32_e32 vcc, s66, v74
	s_barrier
	s_and_saveexec_b64 s[60:61], vcc
	s_cbranch_execz .LBB0_406
	s_lshl_b32 s73, s69, 8
	s_lshl_b32 s50, s71, 7
	s_add_i32 s67, s73, 0x4000
	s_addk_i32 s73, 0x3e00
	s_lshl_b32 s74, s69, 11
	v_lshl_add_u64 v[2:3], v[76:77], 0, s[50:51]
	v_lshrrev_b32_e32 v5, 3, v74
	v_mad_u64_u32 v[10:11], s[64:65], v5, s84, v[70:71]
	v_add_u32_e32 v11, 0x12000, v10
	s_and_b64 vcc, exec, s[48:49]
	s_cbranch_vccnz .Lnastg0_ctx
	v_mov_b32_e32 v4, s87
	ds_read_b64 v[6:7], v4
	s_mul_i32 s62, s71, 0x744
	s_waitcnt lgkmcnt(0)
	v_add_co_u32_e32 v6, vcc, s62, v6
	v_addc_co_u32_e32 v7, vcc, 0, v7, vcc
	v_add_co_u32_e32 v6, vcc, v6, v104
	v_addc_co_u32_e32 v7, vcc, 0, v7, vcc
	s_and_saveexec_b64 s[64:65], s[4:5]
	global_load_dword v226, v[6:7], off
	s_mov_b64 exec, s[64:65]
	s_lshl_b32 s62, s72, 6
	s_add_i32 s62, s62, s74
	v_add_u32_e32 v6, s62, v5
	v_mad_i64_i32 v[6:7], s[64:65], v6, s86, v[2:3]
	global_load_dwordx4 v[108:111], v[6:7], off offset:1536
	s_addk_i32 s62, 0x40
	v_add_u32_e32 v6, s62, v5
	v_mad_i64_i32 v[6:7], s[64:65], v6, s86, v[2:3]
	global_load_dwordx4 v[112:115], v[6:7], off offset:1536
	s_addk_i32 s62, 0x40
	v_add_u32_e32 v6, s62, v5
	v_mad_i64_i32 v[6:7], s[64:65], v6, s86, v[2:3]
	global_load_dwordx4 v[116:119], v[6:7], off offset:1536
	s_addk_i32 s62, 0x40
	v_add_u32_e32 v6, s62, v5
	v_mad_i64_i32 v[6:7], s[64:65], v6, s86, v[2:3]
	global_load_dwordx4 v[120:123], v[6:7], off offset:1536
	s_addk_i32 s62, 0x40
	v_add_u32_e32 v6, s62, v5
	v_mad_i64_i32 v[6:7], s[64:65], v6, s86, v[2:3]
	global_load_dwordx4 v[124:127], v[6:7], off offset:1536
	s_addk_i32 s62, 0x40
	v_add_u32_e32 v6, s62, v5
	v_mad_i64_i32 v[6:7], s[64:65], v6, s86, v[2:3]
	global_load_dwordx4 v[128:131], v[6:7], off offset:1536
	s_addk_i32 s62, 0x40
	v_add_u32_e32 v6, s62, v5
	v_mad_i64_i32 v[6:7], s[64:65], v6, s86, v[2:3]
	global_load_dwordx4 v[132:135], v[6:7], off offset:1536
	s_addk_i32 s62, 0x40
	v_add_u32_e32 v6, s62, v5
	v_mad_i64_i32 v[6:7], s[64:65], v6, s86, v[2:3]
	global_load_dwordx4 v[136:139], v[6:7], off offset:1536
	s_addk_i32 s62, 0x40
	s_add_i32 s62, s73, 0x200
	v_add_u32_e32 v6, s62, v5
	v_mad_i64_i32 v[6:7], s[64:65], v6, s86, v[2:3]
	global_load_dwordx4 v[140:143], v[6:7], off offset:1536
	s_addk_i32 s62, 0x40
	v_add_u32_e32 v6, s62, v5
	v_mad_i64_i32 v[6:7], s[64:65], v6, s86, v[2:3]
	global_load_dwordx4 v[144:147], v[6:7], off offset:1536
	s_addk_i32 s62, 0x40
	v_add_u32_e32 v6, s62, v5
	v_mad_i64_i32 v[6:7], s[64:65], v6, s86, v[2:3]
	global_load_dwordx4 v[148:151], v[6:7], off offset:1536
	s_addk_i32 s62, 0x40
	v_add_u32_e32 v6, s62, v5
	v_mad_i64_i32 v[6:7], s[64:65], v6, s86, v[2:3]
	global_load_dwordx4 v[152:155], v[6:7], off offset:1536
	s_waitcnt vmcnt(11)
	ds_write_b128 v10, v[108:111]
	s_and_saveexec_b64 s[64:65], s[4:5]
	ds_write_b32 v105, v226
	s_mov_b64 exec, s[64:65]
	s_waitcnt vmcnt(10)
	ds_write_b128 v10, v[112:115] offset:9216
	s_waitcnt vmcnt(9)
	ds_write_b128 v10, v[116:119] offset:18432
	s_waitcnt vmcnt(8)
	ds_write_b128 v10, v[120:123] offset:27648
	s_waitcnt vmcnt(7)
	ds_write_b128 v10, v[124:127] offset:36864
	s_waitcnt vmcnt(6)
	ds_write_b128 v10, v[128:131] offset:46080
	s_waitcnt vmcnt(5)
	ds_write_b128 v10, v[132:135] offset:55296
	s_waitcnt vmcnt(4)
	ds_write_b128 v10, v[136:139] offset:64512
	s_waitcnt vmcnt(3)
	ds_write_b128 v11, v[140:143]
	s_waitcnt vmcnt(2)
	ds_write_b128 v11, v[144:147] offset:9216
	s_waitcnt vmcnt(1)
	ds_write_b128 v11, v[148:151] offset:18432
	s_waitcnt vmcnt(0)
	ds_write_b128 v11, v[152:155] offset:27648
	s_branch .LBB0_406

.LBB0_406:
	s_or_b64 exec, exec, s[60:61]
.LBB0_423:
	v_or_b32_e32 v80, s70, v82
	v_mov_b64_e32 v[2:3], s[2:3]
	v_mad_i64_i32 v[2:3], s[48:49], v80, s86, v[2:3]
	s_lshl_b32 s50, s71, 7
	v_lshl_add_u64 v[2:3], v[2:3], 0, s[50:51]
	v_lshl_add_u64 v[2:3], v[2:3], 0, v[66:67]
	global_load_dwordx4 v[6:9], v[2:3], off offset:512
	s_nop 0
	global_load_dwordx4 v[2:5], v[2:3], off offset:576
	s_add_i32 s72, s72, s81
	v_lshl_add_u32 v11, s69, 11, v71
	v_cndmask_b32_e64 v10, 0, 1, s[58:59]
	s_lshl_b32 s62, s71, 6
	v_cmp_ne_u32_e64 s[48:49], 1, v10
	v_lshl_add_u32 v10, s72, 6, v11
	s_mov_b64 s[60:61], 0
	v_mov_b32_e32 v34, 0
	v_mov_b32_e32 v35, 0
	v_mov_b32_e32 v36, 0
	v_mov_b32_e32 v37, 0
	v_mov_b32_e32 v38, 0
	v_mov_b32_e32 v39, 0
	v_mov_b32_e32 v40, 0
	v_mov_b32_e32 v41, 0
	v_mov_b32_e32 v42, 0
	v_mov_b32_e32 v43, 0
	v_mov_b32_e32 v44, 0
	v_mov_b32_e32 v45, 0
	v_mov_b32_e32 v46, 0
	v_mov_b32_e32 v47, 0
	v_mov_b32_e32 v48, 0
	v_mov_b32_e32 v49, 0
	v_mov_b32_e32 v50, 0
	v_mov_b32_e32 v51, 0
	v_mov_b32_e32 v52, 0
	v_mov_b32_e32 v53, 0
	v_mov_b32_e32 v54, 0
	v_mov_b32_e32 v55, 0
	v_mov_b32_e32 v56, 0
	v_mov_b32_e32 v57, 0
	v_mov_b32_e32 v58, 0
	v_mov_b32_e32 v59, 0
	v_mov_b32_e32 v60, 0
	v_mov_b32_e32 v61, 0
	v_mov_b32_e32 v62, 0
	v_mov_b32_e32 v63, 0
	v_mov_b32_e32 v64, 0
	v_mov_b32_e32 v65, 0
	s_andn2_b64 vcc, exec, s[58:59]
	s_cbranch_vccnz .LBB0_439
	v_mov_b64_e32 v[12:13], s[2:3]
	v_mad_i64_i32 v[12:13], s[64:65], v10, s86, v[12:13]
	s_lshl_b32 s50, s62, 1
	v_lshl_add_u64 v[12:13], v[12:13], 0, s[50:51]
	v_lshl_add_u64 v[12:13], v[12:13], 0, v[66:67]
	v_add_co_u32_e32 v14, vcc, 0x30000, v12
	v_addc_co_u32_e32 v15, vcc, 0, v13, vcc
	v_add_co_u32_e32 v16, vcc, 0xc0000, v12
	v_addc_co_u32_e32 v17, vcc, 0, v13, vcc
	v_add_co_u32_e32 v18, vcc, 0xf0000, v12
	v_addc_co_u32_e32 v19, vcc, 0, v13, vcc
	v_add_co_u32_e32 v20, vcc, 0x180000, v12
	v_addc_co_u32_e32 v21, vcc, 0, v13, vcc
	v_add_co_u32_e32 v22, vcc, 0x1b0000, v12
	v_addc_co_u32_e32 v23, vcc, 0, v13, vcc
	v_add_co_u32_e32 v24, vcc, 0x240000, v12
	v_addc_co_u32_e32 v25, vcc, 0, v13, vcc
	v_add_co_u32_e32 v26, vcc, 0x270000, v12
	v_addc_co_u32_e32 v27, vcc, 0, v13, vcc
	global_load_dwordx4 v[160:163], v[12:13], off offset:1024
	global_load_dwordx4 v[164:167], v[14:15], off offset:1024
	global_load_dwordx4 v[168:171], v[16:17], off offset:1024
	global_load_dwordx4 v[172:175], v[18:19], off offset:1024
	global_load_dwordx4 v[176:179], v[20:21], off offset:1024
	global_load_dwordx4 v[180:183], v[22:23], off offset:1024
	global_load_dwordx4 v[184:187], v[24:25], off offset:1024
	global_load_dwordx4 v[188:191], v[26:27], off offset:1024
	global_load_dwordx4 v[192:195], v[12:13], off offset:1088
	global_load_dwordx4 v[196:199], v[14:15], off offset:1088
	global_load_dwordx4 v[200:203], v[16:17], off offset:1088
	global_load_dwordx4 v[204:207], v[18:19], off offset:1088
	global_load_dwordx4 v[208:211], v[20:21], off offset:1088
	global_load_dwordx4 v[214:217], v[22:23], off offset:1088
	global_load_dwordx4 v[218:221], v[24:25], off offset:1088
	global_load_dwordx4 v[222:225], v[26:27], off offset:1088
	s_and_b64 s[60:61], s[56:57], exec

.LBB0_1793:
	v_med3_u32 v2, s68, 4, 28
	s_and_b32 s71, s50, 3
	v_readfirstlane_b32 s72, v2
	s_add_i32 s72, s72, -4
	v_cmp_gt_i32_e32 vcc, s66, v74
	s_barrier
	s_and_saveexec_b64 s[60:61], vcc
	s_cbranch_execz .LBB0_1804
	s_lshl_b32 s73, s69, 8
	s_lshl_b32 s50, s71, 7
	s_add_i32 s67, s73, 0x4000
	s_addk_i32 s73, 0x3e00
	s_lshl_b32 s74, s69, 11
	v_lshl_add_u64 v[2:3], v[76:77], 0, s[50:51]
	v_lshrrev_b32_e32 v5, 3, v74
	v_mad_u64_u32 v[10:11], s[64:65], v5, s84, v[70:71]
	v_add_u32_e32 v11, 0x12000, v10
	s_and_b64 vcc, exec, s[48:49]
	s_cbranch_vccnz .Lnastg1_ctx
	v_mov_b32_e32 v4, s87
	ds_read_b64 v[6:7], v4
	s_mul_i32 s62, s71, 0x744
	s_add_i32 s62, s62, 0x1d10
	s_waitcnt lgkmcnt(0)
	v_add_co_u32_e32 v6, vcc, s62, v6
	v_addc_co_u32_e32 v7, vcc, 0, v7, vcc
	v_add_co_u32_e32 v6, vcc, v6, v104
	v_addc_co_u32_e32 v7, vcc, 0, v7, vcc
	s_and_saveexec_b64 s[64:65], s[4:5]
	global_load_dword v226, v[6:7], off
	s_mov_b64 exec, s[64:65]
	s_lshl_b32 s62, s72, 6
	s_add_i32 s62, s62, s74
	v_add_u32_e32 v6, s62, v5
	v_mad_i64_i32 v[6:7], s[64:65], v6, s86, v[2:3]
	global_load_dwordx4 v[108:111], v[6:7], off offset:1536
	s_addk_i32 s62, 0x40
	v_add_u32_e32 v6, s62, v5
	v_mad_i64_i32 v[6:7], s[64:65], v6, s86, v[2:3]
	global_load_dwordx4 v[112:115], v[6:7], off offset:1536
	s_addk_i32 s62, 0x40
	v_add_u32_e32 v6, s62, v5
	v_mad_i64_i32 v[6:7], s[64:65], v6, s86, v[2:3]
	global_load_dwordx4 v[116:119], v[6:7], off offset:1536
	s_addk_i32 s62, 0x40
	v_add_u32_e32 v6, s62, v5
	v_mad_i64_i32 v[6:7], s[64:65], v6, s86, v[2:3]
	global_load_dwordx4 v[120:123], v[6:7], off offset:1536
	s_addk_i32 s62, 0x40
	v_add_u32_e32 v6, s62, v5
	v_mad_i64_i32 v[6:7], s[64:65], v6, s86, v[2:3]
	global_load_dwordx4 v[124:127], v[6:7], off offset:1536
	s_addk_i32 s62, 0x40
	v_add_u32_e32 v6, s62, v5
	v_mad_i64_i32 v[6:7], s[64:65], v6, s86, v[2:3]
	global_load_dwordx4 v[128:131], v[6:7], off offset:1536
	s_addk_i32 s62, 0x40
	v_add_u32_e32 v6, s62, v5
	v_mad_i64_i32 v[6:7], s[64:65], v6, s86, v[2:3]
	global_load_dwordx4 v[132:135], v[6:7], off offset:1536
	s_addk_i32 s62, 0x40
	v_add_u32_e32 v6, s62, v5
	v_mad_i64_i32 v[6:7], s[64:65], v6, s86, v[2:3]
	global_load_dwordx4 v[136:139], v[6:7], off offset:1536
	s_addk_i32 s62, 0x40
	s_add_i32 s62, s73, 0x200
	v_add_u32_e32 v6, s62, v5
	v_mad_i64_i32 v[6:7], s[64:65], v6, s86, v[2:3]
	global_load_dwordx4 v[140:143], v[6:7], off offset:1536
	s_addk_i32 s62, 0x40
	v_add_u32_e32 v6, s62, v5
	v_mad_i64_i32 v[6:7], s[64:65], v6, s86, v[2:3]
	global_load_dwordx4 v[144:147], v[6:7], off offset:1536
	s_addk_i32 s62, 0x40
	v_add_u32_e32 v6, s62, v5
	v_mad_i64_i32 v[6:7], s[64:65], v6, s86, v[2:3]
	global_load_dwordx4 v[148:151], v[6:7], off offset:1536
	s_addk_i32 s62, 0x40
	v_add_u32_e32 v6, s62, v5
	v_mad_i64_i32 v[6:7], s[64:65], v6, s86, v[2:3]
	global_load_dwordx4 v[152:155], v[6:7], off offset:1536
	s_waitcnt vmcnt(11)
	ds_write_b128 v10, v[108:111]
	s_and_saveexec_b64 s[64:65], s[4:5]
	ds_write_b32 v105, v226
	s_mov_b64 exec, s[64:65]
	s_waitcnt vmcnt(10)
	ds_write_b128 v10, v[112:115] offset:9216
	s_waitcnt vmcnt(9)
	ds_write_b128 v10, v[116:119] offset:18432
	s_waitcnt vmcnt(8)
	ds_write_b128 v10, v[120:123] offset:27648
	s_waitcnt vmcnt(7)
	ds_write_b128 v10, v[124:127] offset:36864
	s_waitcnt vmcnt(6)
	ds_write_b128 v10, v[128:131] offset:46080
	s_waitcnt vmcnt(5)
	ds_write_b128 v10, v[132:135] offset:55296
	s_waitcnt vmcnt(4)
	ds_write_b128 v10, v[136:139] offset:64512
	s_waitcnt vmcnt(3)
	ds_write_b128 v11, v[140:143]
	s_waitcnt vmcnt(2)
	ds_write_b128 v11, v[144:147] offset:9216
	s_waitcnt vmcnt(1)
	ds_write_b128 v11, v[148:151] offset:18432
	s_waitcnt vmcnt(0)
	ds_write_b128 v11, v[152:155] offset:27648
	s_branch .LBB0_1804

.LBB0_1804:
	s_or_b64 exec, exec, s[60:61]
.LBB0_1821:
	v_or_b32_e32 v80, s70, v82
	v_mov_b64_e32 v[2:3], s[2:3]
	v_mad_i64_i32 v[2:3], s[48:49], v80, s86, v[2:3]
	s_lshl_b32 s50, s71, 7
	v_lshl_add_u64 v[2:3], v[2:3], 0, s[50:51]
	v_lshl_add_u64 v[2:3], v[2:3], 0, v[66:67]
	global_load_dwordx4 v[6:9], v[2:3], off offset:512
	s_nop 0
	global_load_dwordx4 v[2:5], v[2:3], off offset:576
	s_add_i32 s72, s72, s81
	v_lshl_add_u32 v11, s69, 11, v71
	v_cndmask_b32_e64 v10, 0, 1, s[58:59]
	s_lshl_b32 s62, s71, 6
	v_cmp_ne_u32_e64 s[48:49], 1, v10
	v_lshl_add_u32 v10, s72, 6, v11
	s_mov_b64 s[60:61], 0
	v_mov_b32_e32 v34, 0
	v_mov_b32_e32 v35, 0
	v_mov_b32_e32 v36, 0
	v_mov_b32_e32 v37, 0
	v_mov_b32_e32 v38, 0
	v_mov_b32_e32 v39, 0
	v_mov_b32_e32 v40, 0
	v_mov_b32_e32 v41, 0
	v_mov_b32_e32 v42, 0
	v_mov_b32_e32 v43, 0
	v_mov_b32_e32 v44, 0
	v_mov_b32_e32 v45, 0
	v_mov_b32_e32 v46, 0
	v_mov_b32_e32 v47, 0
	v_mov_b32_e32 v48, 0
	v_mov_b32_e32 v49, 0
	v_mov_b32_e32 v50, 0
	v_mov_b32_e32 v51, 0
	v_mov_b32_e32 v52, 0
	v_mov_b32_e32 v53, 0
	v_mov_b32_e32 v54, 0
	v_mov_b32_e32 v55, 0
	v_mov_b32_e32 v56, 0
	v_mov_b32_e32 v57, 0
	v_mov_b32_e32 v58, 0
	v_mov_b32_e32 v59, 0
	v_mov_b32_e32 v60, 0
	v_mov_b32_e32 v61, 0
	v_mov_b32_e32 v62, 0
	v_mov_b32_e32 v63, 0
	v_mov_b32_e32 v64, 0
	v_mov_b32_e32 v65, 0
	s_andn2_b64 vcc, exec, s[58:59]
	s_cbranch_vccnz .LBB0_1837
	v_mov_b64_e32 v[12:13], s[2:3]
	v_mad_i64_i32 v[12:13], s[64:65], v10, s86, v[12:13]
	s_lshl_b32 s50, s62, 1
	v_lshl_add_u64 v[12:13], v[12:13], 0, s[50:51]
	v_lshl_add_u64 v[12:13], v[12:13], 0, v[66:67]
	v_add_co_u32_e32 v14, vcc, 0x30000, v12
	v_addc_co_u32_e32 v15, vcc, 0, v13, vcc
	v_add_co_u32_e32 v16, vcc, 0xc0000, v12
	v_addc_co_u32_e32 v17, vcc, 0, v13, vcc
	v_add_co_u32_e32 v18, vcc, 0xf0000, v12
	v_addc_co_u32_e32 v19, vcc, 0, v13, vcc
	v_add_co_u32_e32 v20, vcc, 0x180000, v12
	v_addc_co_u32_e32 v21, vcc, 0, v13, vcc
	v_add_co_u32_e32 v22, vcc, 0x1b0000, v12
	v_addc_co_u32_e32 v23, vcc, 0, v13, vcc
	v_add_co_u32_e32 v24, vcc, 0x240000, v12
	v_addc_co_u32_e32 v25, vcc, 0, v13, vcc
	v_add_co_u32_e32 v26, vcc, 0x270000, v12
	v_addc_co_u32_e32 v27, vcc, 0, v13, vcc
	global_load_dwordx4 v[160:163], v[12:13], off offset:1024
	global_load_dwordx4 v[164:167], v[14:15], off offset:1024
	global_load_dwordx4 v[168:171], v[16:17], off offset:1024
	global_load_dwordx4 v[172:175], v[18:19], off offset:1024
	global_load_dwordx4 v[176:179], v[20:21], off offset:1024
	global_load_dwordx4 v[180:183], v[22:23], off offset:1024
	global_load_dwordx4 v[184:187], v[24:25], off offset:1024
	global_load_dwordx4 v[188:191], v[26:27], off offset:1024
	global_load_dwordx4 v[192:195], v[12:13], off offset:1088
	global_load_dwordx4 v[196:199], v[14:15], off offset:1088
	global_load_dwordx4 v[200:203], v[16:17], off offset:1088
	global_load_dwordx4 v[204:207], v[18:19], off offset:1088
	global_load_dwordx4 v[208:211], v[20:21], off offset:1088
	global_load_dwordx4 v[214:217], v[22:23], off offset:1088
	global_load_dwordx4 v[218:221], v[24:25], off offset:1088
	global_load_dwordx4 v[222:225], v[26:27], off offset:1088
	s_and_b64 s[60:61], s[56:57], exec

.LBB0_3412:
	v_med3_u32 v2, s68, 4, 28
	s_and_b32 s71, s50, 3
	v_readfirstlane_b32 s72, v2
	s_add_i32 s72, s72, -4
	v_cmp_gt_i32_e32 vcc, s66, v74
	s_barrier
	s_and_saveexec_b64 s[60:61], vcc
	s_cbranch_execz .LBB0_3423
	s_lshl_b32 s73, s69, 8
	s_lshl_b32 s50, s71, 7
	s_add_i32 s67, s73, 0x4000
	s_addk_i32 s73, 0x3e00
	s_lshl_b32 s74, s69, 11
	v_lshl_add_u64 v[2:3], v[76:77], 0, s[50:51]
	v_lshrrev_b32_e32 v5, 3, v74
	v_mad_u64_u32 v[10:11], s[64:65], v5, s84, v[70:71]
	v_add_u32_e32 v11, 0x12000, v10
	s_and_b64 vcc, exec, s[48:49]
	s_cbranch_vccnz .Lnastg2_ctx
	v_mov_b32_e32 v4, s87
	ds_read_b64 v[6:7], v4
	s_mul_i32 s62, s71, 0x744
	s_add_i32 s62, s62, 0x3a20
	s_waitcnt lgkmcnt(0)
	v_add_co_u32_e32 v6, vcc, s62, v6
	v_addc_co_u32_e32 v7, vcc, 0, v7, vcc
	v_add_co_u32_e32 v6, vcc, v6, v104
	v_addc_co_u32_e32 v7, vcc, 0, v7, vcc
	s_and_saveexec_b64 s[64:65], s[4:5]
	global_load_dword v226, v[6:7], off
	s_mov_b64 exec, s[64:65]
	s_lshl_b32 s62, s72, 6
	s_add_i32 s62, s62, s74
	v_add_u32_e32 v6, s62, v5
	v_mad_i64_i32 v[6:7], s[64:65], v6, s86, v[2:3]
	global_load_dwordx4 v[108:111], v[6:7], off offset:1536
	s_addk_i32 s62, 0x40
	v_add_u32_e32 v6, s62, v5
	v_mad_i64_i32 v[6:7], s[64:65], v6, s86, v[2:3]
	global_load_dwordx4 v[112:115], v[6:7], off offset:1536
	s_addk_i32 s62, 0x40
	v_add_u32_e32 v6, s62, v5
	v_mad_i64_i32 v[6:7], s[64:65], v6, s86, v[2:3]
	global_load_dwordx4 v[116:119], v[6:7], off offset:1536
	s_addk_i32 s62, 0x40
	v_add_u32_e32 v6, s62, v5
	v_mad_i64_i32 v[6:7], s[64:65], v6, s86, v[2:3]
	global_load_dwordx4 v[120:123], v[6:7], off offset:1536
	s_addk_i32 s62, 0x40
	v_add_u32_e32 v6, s62, v5
	v_mad_i64_i32 v[6:7], s[64:65], v6, s86, v[2:3]
	global_load_dwordx4 v[124:127], v[6:7], off offset:1536
	s_addk_i32 s62, 0x40
	v_add_u32_e32 v6, s62, v5
	v_mad_i64_i32 v[6:7], s[64:65], v6, s86, v[2:3]
	global_load_dwordx4 v[128:131], v[6:7], off offset:1536
	s_addk_i32 s62, 0x40
	v_add_u32_e32 v6, s62, v5
	v_mad_i64_i32 v[6:7], s[64:65], v6, s86, v[2:3]
	global_load_dwordx4 v[132:135], v[6:7], off offset:1536
	s_addk_i32 s62, 0x40
	v_add_u32_e32 v6, s62, v5
	v_mad_i64_i32 v[6:7], s[64:65], v6, s86, v[2:3]
	global_load_dwordx4 v[136:139], v[6:7], off offset:1536
	s_addk_i32 s62, 0x40
	s_add_i32 s62, s73, 0x200
	v_add_u32_e32 v6, s62, v5
	v_mad_i64_i32 v[6:7], s[64:65], v6, s86, v[2:3]
	global_load_dwordx4 v[140:143], v[6:7], off offset:1536
	s_addk_i32 s62, 0x40
	v_add_u32_e32 v6, s62, v5
	v_mad_i64_i32 v[6:7], s[64:65], v6, s86, v[2:3]
	global_load_dwordx4 v[144:147], v[6:7], off offset:1536
	s_addk_i32 s62, 0x40
	v_add_u32_e32 v6, s62, v5
	v_mad_i64_i32 v[6:7], s[64:65], v6, s86, v[2:3]
	global_load_dwordx4 v[148:151], v[6:7], off offset:1536
	s_addk_i32 s62, 0x40
	v_add_u32_e32 v6, s62, v5
	v_mad_i64_i32 v[6:7], s[64:65], v6, s86, v[2:3]
	global_load_dwordx4 v[152:155], v[6:7], off offset:1536
	s_waitcnt vmcnt(11)
	ds_write_b128 v10, v[108:111]
	s_and_saveexec_b64 s[64:65], s[4:5]
	ds_write_b32 v105, v226
	s_mov_b64 exec, s[64:65]
	s_waitcnt vmcnt(10)
	ds_write_b128 v10, v[112:115] offset:9216
	s_waitcnt vmcnt(9)
	ds_write_b128 v10, v[116:119] offset:18432
	s_waitcnt vmcnt(8)
	ds_write_b128 v10, v[120:123] offset:27648
	s_waitcnt vmcnt(7)
	ds_write_b128 v10, v[124:127] offset:36864
	s_waitcnt vmcnt(6)
	ds_write_b128 v10, v[128:131] offset:46080
	s_waitcnt vmcnt(5)
	ds_write_b128 v10, v[132:135] offset:55296
	s_waitcnt vmcnt(4)
	ds_write_b128 v10, v[136:139] offset:64512
	s_waitcnt vmcnt(3)
	ds_write_b128 v11, v[140:143]
	s_waitcnt vmcnt(2)
	ds_write_b128 v11, v[144:147] offset:9216
	s_waitcnt vmcnt(1)
	ds_write_b128 v11, v[148:151] offset:18432
	s_waitcnt vmcnt(0)
	ds_write_b128 v11, v[152:155] offset:27648
	s_branch .LBB0_3423

.LBB0_3423:
	s_or_b64 exec, exec, s[60:61]
.LBB0_3440:
	v_or_b32_e32 v80, s70, v82
	v_mov_b64_e32 v[2:3], s[2:3]
	v_mad_i64_i32 v[2:3], s[48:49], v80, s86, v[2:3]
	s_lshl_b32 s50, s71, 7
	v_lshl_add_u64 v[2:3], v[2:3], 0, s[50:51]
	v_lshl_add_u64 v[2:3], v[2:3], 0, v[66:67]
	global_load_dwordx4 v[6:9], v[2:3], off offset:512
	s_nop 0
	global_load_dwordx4 v[2:5], v[2:3], off offset:576
	s_add_i32 s72, s72, s81
	v_lshl_add_u32 v11, s69, 11, v71
	v_cndmask_b32_e64 v10, 0, 1, s[58:59]
	s_lshl_b32 s62, s71, 6
	v_cmp_ne_u32_e64 s[48:49], 1, v10
	v_lshl_add_u32 v10, s72, 6, v11
	s_mov_b64 s[60:61], 0
	v_mov_b32_e32 v34, 0
	v_mov_b32_e32 v35, 0
	v_mov_b32_e32 v36, 0
	v_mov_b32_e32 v37, 0
	v_mov_b32_e32 v38, 0
	v_mov_b32_e32 v39, 0
	v_mov_b32_e32 v40, 0
	v_mov_b32_e32 v41, 0
	v_mov_b32_e32 v42, 0
	v_mov_b32_e32 v43, 0
	v_mov_b32_e32 v44, 0
	v_mov_b32_e32 v45, 0
	v_mov_b32_e32 v46, 0
	v_mov_b32_e32 v47, 0
	v_mov_b32_e32 v48, 0
	v_mov_b32_e32 v49, 0
	v_mov_b32_e32 v50, 0
	v_mov_b32_e32 v51, 0
	v_mov_b32_e32 v52, 0
	v_mov_b32_e32 v53, 0
	v_mov_b32_e32 v54, 0
	v_mov_b32_e32 v55, 0
	v_mov_b32_e32 v56, 0
	v_mov_b32_e32 v57, 0
	v_mov_b32_e32 v58, 0
	v_mov_b32_e32 v59, 0
	v_mov_b32_e32 v60, 0
	v_mov_b32_e32 v61, 0
	v_mov_b32_e32 v62, 0
	v_mov_b32_e32 v63, 0
	v_mov_b32_e32 v64, 0
	v_mov_b32_e32 v65, 0
	s_andn2_b64 vcc, exec, s[58:59]
	s_cbranch_vccnz .LBB0_3456
	v_mov_b64_e32 v[12:13], s[2:3]
	v_mad_i64_i32 v[12:13], s[64:65], v10, s86, v[12:13]
	s_lshl_b32 s50, s62, 1
	v_lshl_add_u64 v[12:13], v[12:13], 0, s[50:51]
	v_lshl_add_u64 v[12:13], v[12:13], 0, v[66:67]
	v_add_co_u32_e32 v14, vcc, 0x30000, v12
	v_addc_co_u32_e32 v15, vcc, 0, v13, vcc
	v_add_co_u32_e32 v16, vcc, 0xc0000, v12
	v_addc_co_u32_e32 v17, vcc, 0, v13, vcc
	v_add_co_u32_e32 v18, vcc, 0xf0000, v12
	v_addc_co_u32_e32 v19, vcc, 0, v13, vcc
	v_add_co_u32_e32 v20, vcc, 0x180000, v12
	v_addc_co_u32_e32 v21, vcc, 0, v13, vcc
	v_add_co_u32_e32 v22, vcc, 0x1b0000, v12
	v_addc_co_u32_e32 v23, vcc, 0, v13, vcc
	v_add_co_u32_e32 v24, vcc, 0x240000, v12
	v_addc_co_u32_e32 v25, vcc, 0, v13, vcc
	v_add_co_u32_e32 v26, vcc, 0x270000, v12
	v_addc_co_u32_e32 v27, vcc, 0, v13, vcc
	global_load_dwordx4 v[160:163], v[12:13], off offset:1024
	global_load_dwordx4 v[164:167], v[14:15], off offset:1024
	global_load_dwordx4 v[168:171], v[16:17], off offset:1024
	global_load_dwordx4 v[172:175], v[18:19], off offset:1024
	global_load_dwordx4 v[176:179], v[20:21], off offset:1024
	global_load_dwordx4 v[180:183], v[22:23], off offset:1024
	global_load_dwordx4 v[184:187], v[24:25], off offset:1024
	global_load_dwordx4 v[188:191], v[26:27], off offset:1024
	global_load_dwordx4 v[192:195], v[12:13], off offset:1088
	global_load_dwordx4 v[196:199], v[14:15], off offset:1088
	global_load_dwordx4 v[200:203], v[16:17], off offset:1088
	global_load_dwordx4 v[204:207], v[18:19], off offset:1088
	global_load_dwordx4 v[208:211], v[20:21], off offset:1088
	global_load_dwordx4 v[214:217], v[22:23], off offset:1088
	global_load_dwordx4 v[218:221], v[24:25], off offset:1088
	global_load_dwordx4 v[222:225], v[26:27], off offset:1088
	s_and_b64 s[60:61], s[56:57], exec
